# MoE converters: the 4 copy-out LDS reads of a K-tile issued together (4 register quads) instead of read-wait-store ladders
# baseline (speedup 1.0000x reference)
.Lcw_gu:
	s_waitcnt vmcnt(34)
	v_cvt_scalef32_pk_fp8_f32 v152, v0, v4, s22
	s_waitcnt vmcnt(30)
	v_cvt_scalef32_pk_fp8_f32 v153, v16, v20, s22
	s_waitcnt vmcnt(26)
	v_cvt_scalef32_pk_fp8_f32 v154, v32, v36, s22
	s_waitcnt vmcnt(22)
	v_cvt_scalef32_pk_fp8_f32 v155, v48, v52, s22
	v_cvt_scalef32_pk_fp8_f32 v152, v8, v12, s22 op_sel:[0,0,0,1]
	v_cvt_scalef32_pk_fp8_f32 v153, v24, v28, s22 op_sel:[0,0,0,1]
	v_cvt_scalef32_pk_fp8_f32 v154, v40, v44, s22 op_sel:[0,0,0,1]
	s_waitcnt vmcnt(20)
	v_cvt_scalef32_pk_fp8_f32 v155, v56, v60, s22 op_sel:[0,0,0,1]
	ds_write_b128 v141, v[152:155]
	v_mov_b32_e32 v152, v123
	v_mov_b32_e32 v153, v123
	v_mov_b32_e32 v154, v123
	v_mov_b32_e32 v155, v123
	v_cvt_scalef32_pk_fp8_f32 v152, v1, v5, s22
	v_cvt_scalef32_pk_fp8_f32 v153, v17, v21, s22
	v_cvt_scalef32_pk_fp8_f32 v154, v33, v37, s22
	v_cvt_scalef32_pk_fp8_f32 v155, v49, v53, s22
	v_cvt_scalef32_pk_fp8_f32 v152, v9, v13, s22 op_sel:[0,0,0,1]
	v_cvt_scalef32_pk_fp8_f32 v153, v25, v29, s22 op_sel:[0,0,0,1]
	v_cvt_scalef32_pk_fp8_f32 v154, v41, v45, s22 op_sel:[0,0,0,1]
	v_cvt_scalef32_pk_fp8_f32 v155, v57, v61, s22 op_sel:[0,0,0,1]
	ds_write_b128 v141, v[152:155] offset:128
	v_mov_b32_e32 v152, v123
	v_mov_b32_e32 v0, v123
	v_cvt_scalef32_pk_fp8_f32 v152, v2, v6, s22
	v_mov_b32_e32 v153, v123
	v_mov_b32_e32 v154, v123
	v_mov_b32_e32 v155, v123
	v_cvt_scalef32_pk_fp8_f32 v0, v3, v7, s22
	v_mov_b32_e32 v1, v123
	v_mov_b32_e32 v2, v123
	v_mov_b32_e32 v3, v123
	v_cvt_scalef32_pk_fp8_f32 v153, v18, v22, s22
	v_cvt_scalef32_pk_fp8_f32 v154, v34, v38, s22
	v_cvt_scalef32_pk_fp8_f32 v155, v50, v54, s22
	v_cvt_scalef32_pk_fp8_f32 v1, v19, v23, s22
	v_cvt_scalef32_pk_fp8_f32 v2, v35, v39, s22
	v_cvt_scalef32_pk_fp8_f32 v3, v51, v55, s22
	v_cvt_scalef32_pk_fp8_f32 v152, v10, v14, s22 op_sel:[0,0,0,1]
	v_cvt_scalef32_pk_fp8_f32 v153, v26, v30, s22 op_sel:[0,0,0,1]
	v_cvt_scalef32_pk_fp8_f32 v154, v42, v46, s22 op_sel:[0,0,0,1]
	v_cvt_scalef32_pk_fp8_f32 v155, v58, v62, s22 op_sel:[0,0,0,1]
	v_cvt_scalef32_pk_fp8_f32 v0, v11, v15, s22 op_sel:[0,0,0,1]
	v_cvt_scalef32_pk_fp8_f32 v1, v27, v31, s22 op_sel:[0,0,0,1]
	v_cvt_scalef32_pk_fp8_f32 v2, v43, v47, s22 op_sel:[0,0,0,1]
	v_cvt_scalef32_pk_fp8_f32 v3, v59, v63, s22 op_sel:[0,0,0,1]
	ds_write_b128 v142, v[152:155]
	ds_write_b128 v143, v[0:3]
	s_waitcnt lgkmcnt(0)
	s_barrier
; #define G_SCHED __builtin_amdgcn_sched_barrier(0)
; #define CI_LOAD(R, kt) do { _Pragma("unroll") for (int _j = 0; _j < 16; ++_j) R[_j] = __builtin_nontemporal_load((const f32x4*)(src + (size_t)((kt) * 128 + _j) * LDB)); } while (0)
; template <int LDB>
; __device__ __forceinline__ void convert_image(const float* __restrict__ W, int col0, int col1, unsigned char* __restrict__ img, LAS3 char* lds, int wid) {
;     ...
;     f32x4 ra[16], rb[16];
;     CI_LOAD(ra, 0);
;     for (int kt = 0; kt < 16; kt += 2) {
;         CI_LOAD(rb, kt + 1); G_SCHED;
;         CI_CONV(ra, kt); G_SCHED;
;         CI_LOAD(ra, (kt + 2 < 16) ? kt + 2 : 15); G_SCHED;
;         CI_CONV(rb, kt + 1); G_SCHED;
	ds_read_b128 v[0:3], v144
	ds_read_b128 v[4:7], v144 offset:1024
	ds_read_b128 v[8:11], v144 offset:2048
	ds_read_b128 v[12:15], v144 offset:3072
	s_nop 3
	s_waitcnt lgkmcnt(3)
	global_store_dwordx4 v137, v[0:3], s[0:1] sc1
	s_waitcnt lgkmcnt(2)
	global_store_dwordx4 v138, v[4:7], s[0:1] sc1
	s_waitcnt lgkmcnt(1)
	global_store_dwordx4 v139, v[8:11], s[0:1] sc1
	s_waitcnt lgkmcnt(0)
	global_store_dwordx4 v140, v[12:15], s[0:1] sc1
	s_nop 1
	s_min_u32 s4, s13, 13
	s_lshl_b32 s4, s4, 21
	v_lshl_add_u64 v[56:57], v[132:133], 0, s[4:5]
	s_mov_b32 s4, 0x400000
	v_add_co_u32_e32 v0, vcc, s4, v56
	s_mov_b32 s4, 0x404000
	s_nop 0
	v_addc_co_u32_e32 v1, vcc, 0, v57, vcc
	v_add_co_u32_e32 v4, vcc, s4, v56
	s_mov_b32 s4, 0x408000
	s_nop 0
	v_addc_co_u32_e32 v5, vcc, 0, v57, vcc
	v_add_co_u32_e32 v8, vcc, s4, v56
	s_mov_b32 s4, 0x40c000
	s_nop 0
	v_addc_co_u32_e32 v9, vcc, 0, v57, vcc
	v_add_co_u32_e32 v12, vcc, s4, v56
	s_mov_b32 s4, 0x410000
	s_nop 0
	v_addc_co_u32_e32 v13, vcc, 0, v57, vcc
	v_add_co_u32_e32 v16, vcc, s4, v56
	s_mov_b32 s4, 0x414000
	s_nop 0
	v_addc_co_u32_e32 v17, vcc, 0, v57, vcc
	v_add_co_u32_e32 v20, vcc, s4, v56
	s_mov_b32 s4, 0x418000
	s_nop 0
	v_addc_co_u32_e32 v21, vcc, 0, v57, vcc
	v_add_co_u32_e32 v24, vcc, s4, v56
	s_mov_b32 s4, 0x41c000
	s_nop 0
	v_addc_co_u32_e32 v25, vcc, 0, v57, vcc
	v_add_co_u32_e32 v28, vcc, s4, v56
	s_mov_b32 s4, 0x420000
	s_nop 0
	v_addc_co_u32_e32 v29, vcc, 0, v57, vcc
	v_add_co_u32_e32 v32, vcc, s4, v56
	s_mov_b32 s4, 0x424000
	s_nop 0
	v_addc_co_u32_e32 v33, vcc, 0, v57, vcc
	v_add_co_u32_e32 v36, vcc, s4, v56
	s_mov_b32 s4, 0x428000
	s_nop 0
	v_addc_co_u32_e32 v37, vcc, 0, v57, vcc
	v_add_co_u32_e32 v40, vcc, s4, v56
	s_mov_b32 s4, 0x42c000
	s_nop 0
	v_addc_co_u32_e32 v41, vcc, 0, v57, vcc
	v_add_co_u32_e32 v44, vcc, s4, v56
	s_mov_b32 s4, 0x430000
	s_nop 0
	v_addc_co_u32_e32 v45, vcc, 0, v57, vcc
	v_add_co_u32_e32 v48, vcc, s4, v56
	s_mov_b32 s4, 0x434000
	s_nop 0
	v_addc_co_u32_e32 v49, vcc, 0, v57, vcc
	v_add_co_u32_e32 v52, vcc, s4, v56
	s_mov_b32 s4, 0x438000
	s_nop 0
	v_addc_co_u32_e32 v53, vcc, 0, v57, vcc
	v_add_co_u32_e32 v58, vcc, s4, v56
	s_mov_b32 s4, 0x43c000
	s_nop 0
	v_addc_co_u32_e32 v59, vcc, 0, v57, vcc
	v_add_co_u32_e32 v60, vcc, s4, v56
	global_load_dwordx4 v[0:3], v[0:1], off nt
	s_nop 0
	global_load_dwordx4 v[4:7], v[4:5], off nt
	v_addc_co_u32_e32 v61, vcc, 0, v57, vcc
	global_load_dwordx4 v[8:11], v[8:9], off nt
	s_nop 0
	global_load_dwordx4 v[12:15], v[12:13], off nt
	s_nop 0
	global_load_dwordx4 v[16:19], v[16:17], off nt
	s_nop 0
	global_load_dwordx4 v[20:23], v[20:21], off nt
	s_nop 0
	global_load_dwordx4 v[24:27], v[24:25], off nt
	s_nop 0
	global_load_dwordx4 v[28:31], v[28:29], off nt
	s_nop 0
	global_load_dwordx4 v[32:35], v[32:33], off nt
	s_nop 0
	global_load_dwordx4 v[36:39], v[36:37], off nt
	s_nop 0
	global_load_dwordx4 v[40:43], v[40:41], off nt
	s_nop 0
	global_load_dwordx4 v[44:47], v[44:45], off nt
	s_nop 0
	global_load_dwordx4 v[48:51], v[48:49], off nt
	s_nop 0
	global_load_dwordx4 v[52:55], v[52:53], off nt
	s_nop 0
	global_load_dwordx4 v[56:59], v[58:59], off nt
	s_nop 0
	global_load_dwordx4 v[60:63], v[60:61], off nt
	v_mov_b32_e32 v152, v123
	v_mov_b32_e32 v153, v123
	v_mov_b32_e32 v154, v123
	v_mov_b32_e32 v155, v123
	s_waitcnt vmcnt(21)
	v_cvt_scalef32_pk_fp8_f32 v152, v128, v64, s22
	v_cvt_scalef32_pk_fp8_f32 v153, v76, v80, s22
	v_cvt_scalef32_pk_fp8_f32 v154, v92, v96, s22
	v_cvt_scalef32_pk_fp8_f32 v155, v108, v112, s22
	v_cvt_scalef32_pk_fp8_f32 v152, v68, v72, s22 op_sel:[0,0,0,1]
	v_cvt_scalef32_pk_fp8_f32 v153, v84, v88, s22 op_sel:[0,0,0,1]
	v_cvt_scalef32_pk_fp8_f32 v154, v100, v104, s22 op_sel:[0,0,0,1]
	s_waitcnt vmcnt(20)
	v_cvt_scalef32_pk_fp8_f32 v155, v116, v124, s22 op_sel:[0,0,0,1]
	ds_write_b128 v141, v[152:155] offset:32768
	v_mov_b32_e32 v152, v123
	v_mov_b32_e32 v153, v123
	v_mov_b32_e32 v154, v123
	v_mov_b32_e32 v155, v123
	v_cvt_scalef32_pk_fp8_f32 v152, v129, v65, s22
	v_cvt_scalef32_pk_fp8_f32 v153, v77, v81, s22
	v_cvt_scalef32_pk_fp8_f32 v154, v93, v97, s22
	v_cvt_scalef32_pk_fp8_f32 v155, v109, v113, s22
	v_cvt_scalef32_pk_fp8_f32 v152, v69, v73, s22 op_sel:[0,0,0,1]
	v_cvt_scalef32_pk_fp8_f32 v153, v85, v89, s22 op_sel:[0,0,0,1]
	v_cvt_scalef32_pk_fp8_f32 v154, v101, v105, s22 op_sel:[0,0,0,1]
	v_cvt_scalef32_pk_fp8_f32 v155, v117, v125, s22 op_sel:[0,0,0,1]
	ds_write_b128 v141, v[152:155] offset:32896
	v_mov_b32_e32 v152, v123
	v_mov_b32_e32 v153, v123
	v_mov_b32_e32 v154, v123
	v_mov_b32_e32 v155, v123
	v_mov_b32_e32 v120, v123
	v_mov_b32_e32 v121, v123
	v_mov_b32_e32 v122, v123
	v_cvt_scalef32_pk_fp8_f32 v152, v130, v66, s22
	v_cvt_scalef32_pk_fp8_f32 v153, v78, v82, s22
	v_cvt_scalef32_pk_fp8_f32 v154, v94, v98, s22
	v_cvt_scalef32_pk_fp8_f32 v155, v110, v114, s22
	v_cvt_scalef32_pk_fp8_f32 v120, v131, v67, s22
	v_cvt_scalef32_pk_fp8_f32 v121, v79, v83, s22
	v_cvt_scalef32_pk_fp8_f32 v122, v95, v99, s22
	v_cvt_scalef32_pk_fp8_f32 v123, v111, v115, s22
	v_cvt_scalef32_pk_fp8_f32 v152, v70, v74, s22 op_sel:[0,0,0,1]
	v_cvt_scalef32_pk_fp8_f32 v153, v86, v90, s22 op_sel:[0,0,0,1]
	v_cvt_scalef32_pk_fp8_f32 v154, v102, v106, s22 op_sel:[0,0,0,1]
	v_cvt_scalef32_pk_fp8_f32 v155, v118, v126, s22 op_sel:[0,0,0,1]
	v_cvt_scalef32_pk_fp8_f32 v120, v71, v75, s22 op_sel:[0,0,0,1]
	v_cvt_scalef32_pk_fp8_f32 v121, v87, v91, s22 op_sel:[0,0,0,1]
	v_cvt_scalef32_pk_fp8_f32 v122, v103, v107, s22 op_sel:[0,0,0,1]
	v_cvt_scalef32_pk_fp8_f32 v123, v119, v127, s22 op_sel:[0,0,0,1]
	s_add_u32 s24, s0, 0x8000
	ds_write_b128 v142, v[152:155] offset:32768
	ds_write_b128 v143, v[120:123] offset:32768
	s_waitcnt lgkmcnt(0)
	s_barrier
	s_addc_u32 s25, s1, 0
	ds_read_b128 v[64:67], v144 offset:32768
	ds_read_b128 v[68:71], v144 offset:33792
	ds_read_b128 v[72:75], v144 offset:34816
	ds_read_b128 v[76:79], v144 offset:35840
	s_nop 3
	s_waitcnt lgkmcnt(3)
	global_store_dwordx4 v137, v[64:67], s[24:25] sc1
	s_waitcnt lgkmcnt(2)
	global_store_dwordx4 v138, v[68:71], s[24:25] sc1
	s_waitcnt lgkmcnt(1)
	global_store_dwordx4 v139, v[72:75], s[24:25] sc1
	s_waitcnt lgkmcnt(0)
	global_store_dwordx4 v140, v[76:79], s[24:25] sc1
	s_nop 1
	s_add_u32 s0, s0, 0x10000
	s_addc_u32 s1, s1, 0
	s_mov_b64 s[24:25], 0x400000
	s_cmp_lt_u32 s13, 14
	v_lshl_add_u64 v[134:135], v[134:135], 0, s[24:25]
	s_cbranch_scc1 .LBB0_490

.Lcw_dn:
	s_waitcnt vmcnt(34)
	v_cvt_scalef32_pk_fp8_f32 v148, v0, v4, s17
	s_waitcnt vmcnt(30)
	v_cvt_scalef32_pk_fp8_f32 v149, v16, v20, s17
	s_waitcnt vmcnt(26)
	v_cvt_scalef32_pk_fp8_f32 v150, v32, v36, s17
	s_waitcnt vmcnt(22)
	v_cvt_scalef32_pk_fp8_f32 v151, v48, v52, s17
	v_cvt_scalef32_pk_fp8_f32 v148, v8, v12, s17 op_sel:[0,0,0,1]
	v_cvt_scalef32_pk_fp8_f32 v149, v24, v28, s17 op_sel:[0,0,0,1]
	v_cvt_scalef32_pk_fp8_f32 v150, v40, v44, s17 op_sel:[0,0,0,1]
	s_waitcnt vmcnt(20)
	v_cvt_scalef32_pk_fp8_f32 v151, v56, v60, s17 op_sel:[0,0,0,1]
	ds_write_b128 v141, v[148:151]
	v_mov_b32_e32 v148, v123
	v_mov_b32_e32 v149, v123
	v_mov_b32_e32 v150, v123
	v_mov_b32_e32 v151, v123
	v_cvt_scalef32_pk_fp8_f32 v148, v1, v5, s17
	v_cvt_scalef32_pk_fp8_f32 v149, v17, v21, s17
	v_cvt_scalef32_pk_fp8_f32 v150, v33, v37, s17
	v_cvt_scalef32_pk_fp8_f32 v151, v49, v53, s17
	v_cvt_scalef32_pk_fp8_f32 v148, v9, v13, s17 op_sel:[0,0,0,1]
	v_cvt_scalef32_pk_fp8_f32 v149, v25, v29, s17 op_sel:[0,0,0,1]
	v_cvt_scalef32_pk_fp8_f32 v150, v41, v45, s17 op_sel:[0,0,0,1]
	v_cvt_scalef32_pk_fp8_f32 v151, v57, v61, s17 op_sel:[0,0,0,1]
	ds_write_b128 v141, v[148:151] offset:128
	v_mov_b32_e32 v148, v123
	v_mov_b32_e32 v0, v123
	v_cvt_scalef32_pk_fp8_f32 v148, v2, v6, s17
	v_mov_b32_e32 v149, v123
	v_mov_b32_e32 v150, v123
	v_mov_b32_e32 v151, v123
	v_cvt_scalef32_pk_fp8_f32 v0, v3, v7, s17
	v_mov_b32_e32 v1, v123
	v_mov_b32_e32 v2, v123
	v_mov_b32_e32 v3, v123
	v_cvt_scalef32_pk_fp8_f32 v149, v18, v22, s17
	v_cvt_scalef32_pk_fp8_f32 v150, v34, v38, s17
	v_cvt_scalef32_pk_fp8_f32 v151, v50, v54, s17
	v_cvt_scalef32_pk_fp8_f32 v1, v19, v23, s17
	v_cvt_scalef32_pk_fp8_f32 v2, v35, v39, s17
	v_cvt_scalef32_pk_fp8_f32 v3, v51, v55, s17
	v_cvt_scalef32_pk_fp8_f32 v148, v10, v14, s17 op_sel:[0,0,0,1]
	v_cvt_scalef32_pk_fp8_f32 v149, v26, v30, s17 op_sel:[0,0,0,1]
	v_cvt_scalef32_pk_fp8_f32 v150, v42, v46, s17 op_sel:[0,0,0,1]
	v_cvt_scalef32_pk_fp8_f32 v151, v58, v62, s17 op_sel:[0,0,0,1]
	v_cvt_scalef32_pk_fp8_f32 v0, v11, v15, s17 op_sel:[0,0,0,1]
	v_cvt_scalef32_pk_fp8_f32 v1, v27, v31, s17 op_sel:[0,0,0,1]
	v_cvt_scalef32_pk_fp8_f32 v2, v43, v47, s17 op_sel:[0,0,0,1]
	v_cvt_scalef32_pk_fp8_f32 v3, v59, v63, s17 op_sel:[0,0,0,1]
	ds_write_b128 v142, v[148:151]
	ds_write_b128 v143, v[0:3]
	s_waitcnt lgkmcnt(0)
	s_barrier
; #define G_SCHED __builtin_amdgcn_sched_barrier(0)
; #define CI_LOAD(R, kt) do { _Pragma("unroll") for (int _j = 0; _j < 16; ++_j) R[_j] = __builtin_nontemporal_load((const f32x4*)(src + (size_t)((kt) * 128 + _j) * LDB)); } while (0)
; template <int LDB>
; __device__ __forceinline__ void convert_image(const float* __restrict__ W, int col0, int col1, unsigned char* __restrict__ img, LAS3 char* lds, int wid) {
;     ...
;     f32x4 ra[16], rb[16];
;     CI_LOAD(ra, 0);
;     for (int kt = 0; kt < 16; kt += 2) {
;         CI_LOAD(rb, kt + 1); G_SCHED;
;         CI_CONV(ra, kt); G_SCHED;
;         CI_LOAD(ra, (kt + 2 < 16) ? kt + 2 : 15); G_SCHED;
;         CI_CONV(rb, kt + 1); G_SCHED;
	ds_read_b128 v[0:3], v152
	ds_read_b128 v[4:7], v152 offset:1024
	ds_read_b128 v[8:11], v152 offset:2048
	ds_read_b128 v[12:15], v152 offset:3072
	s_nop 3
	s_waitcnt lgkmcnt(3)
	global_store_dwordx4 v137, v[0:3], s[0:1] sc1
	s_waitcnt lgkmcnt(2)
	global_store_dwordx4 v138, v[4:7], s[0:1] sc1
	s_waitcnt lgkmcnt(1)
	global_store_dwordx4 v139, v[8:11], s[0:1] sc1
	s_waitcnt lgkmcnt(0)
	global_store_dwordx4 v140, v[12:15], s[0:1] sc1
	s_nop 1
	s_min_u32 s4, s14, 13
	s_lshl_b32 s4, s4, 20
	v_lshl_add_u64 v[56:57], v[132:133], 0, s[4:5]
	s_mov_b32 s4, 0x200000
	v_add_co_u32_e32 v0, vcc, s4, v56
	s_mov_b32 s4, 0x202000
	s_nop 0
	v_addc_co_u32_e32 v1, vcc, 0, v57, vcc
	v_add_co_u32_e32 v4, vcc, s4, v56
	s_mov_b32 s4, 0x204000
	s_nop 0
	v_addc_co_u32_e32 v5, vcc, 0, v57, vcc
	v_add_co_u32_e32 v8, vcc, s4, v56
	s_mov_b32 s4, 0x206000
	s_nop 0
	v_addc_co_u32_e32 v9, vcc, 0, v57, vcc
	v_add_co_u32_e32 v12, vcc, s4, v56
	s_mov_b32 s4, 0x208000
	s_nop 0
	v_addc_co_u32_e32 v13, vcc, 0, v57, vcc
	v_add_co_u32_e32 v16, vcc, s4, v56
	s_mov_b32 s4, 0x20a000
	s_nop 0
	v_addc_co_u32_e32 v17, vcc, 0, v57, vcc
	v_add_co_u32_e32 v20, vcc, s4, v56
	s_mov_b32 s4, 0x20c000
	s_nop 0
	v_addc_co_u32_e32 v21, vcc, 0, v57, vcc
	v_add_co_u32_e32 v24, vcc, s4, v56
	s_mov_b32 s4, 0x20e000
	s_nop 0
	v_addc_co_u32_e32 v25, vcc, 0, v57, vcc
	v_add_co_u32_e32 v28, vcc, s4, v56
	s_mov_b32 s4, 0x210000
	s_nop 0
	v_addc_co_u32_e32 v29, vcc, 0, v57, vcc
	v_add_co_u32_e32 v32, vcc, s4, v56
	s_mov_b32 s4, 0x212000
	s_nop 0
	v_addc_co_u32_e32 v33, vcc, 0, v57, vcc
	v_add_co_u32_e32 v36, vcc, s4, v56
	s_mov_b32 s4, 0x214000
	s_nop 0
	v_addc_co_u32_e32 v37, vcc, 0, v57, vcc
	v_add_co_u32_e32 v40, vcc, s4, v56
	s_mov_b32 s4, 0x216000
	s_nop 0
	v_addc_co_u32_e32 v41, vcc, 0, v57, vcc
	v_add_co_u32_e32 v44, vcc, s4, v56
	s_mov_b32 s4, 0x218000
	s_nop 0
	v_addc_co_u32_e32 v45, vcc, 0, v57, vcc
	v_add_co_u32_e32 v48, vcc, s4, v56
	s_mov_b32 s4, 0x21a000
	s_nop 0
	v_addc_co_u32_e32 v49, vcc, 0, v57, vcc
	v_add_co_u32_e32 v52, vcc, s4, v56
	s_mov_b32 s4, 0x21c000
	s_nop 0
	v_addc_co_u32_e32 v53, vcc, 0, v57, vcc
	v_add_co_u32_e32 v58, vcc, s4, v56
	s_mov_b32 s4, 0x21e000
	s_nop 0
	v_addc_co_u32_e32 v59, vcc, 0, v57, vcc
	v_add_co_u32_e32 v60, vcc, s4, v56
	global_load_dwordx4 v[0:3], v[0:1], off nt
	s_nop 0
	global_load_dwordx4 v[4:7], v[4:5], off nt
	v_addc_co_u32_e32 v61, vcc, 0, v57, vcc
	global_load_dwordx4 v[8:11], v[8:9], off nt
	s_nop 0
	global_load_dwordx4 v[12:15], v[12:13], off nt
	s_nop 0
	global_load_dwordx4 v[16:19], v[16:17], off nt
	s_nop 0
	global_load_dwordx4 v[20:23], v[20:21], off nt
	s_nop 0
	global_load_dwordx4 v[24:27], v[24:25], off nt
	s_nop 0
	global_load_dwordx4 v[28:31], v[28:29], off nt
	s_nop 0
	global_load_dwordx4 v[32:35], v[32:33], off nt
	s_nop 0
	global_load_dwordx4 v[36:39], v[36:37], off nt
	s_nop 0
	global_load_dwordx4 v[40:43], v[40:41], off nt
	s_nop 0
	global_load_dwordx4 v[44:47], v[44:45], off nt
	s_nop 0
	global_load_dwordx4 v[48:51], v[48:49], off nt
	s_nop 0
	global_load_dwordx4 v[52:55], v[52:53], off nt
	s_nop 0
	global_load_dwordx4 v[56:59], v[58:59], off nt
	s_nop 0
	global_load_dwordx4 v[60:63], v[60:61], off nt
	v_mov_b32_e32 v148, v123
	v_mov_b32_e32 v149, v123
	v_mov_b32_e32 v150, v123
	v_mov_b32_e32 v151, v123
	s_waitcnt vmcnt(21)
	v_cvt_scalef32_pk_fp8_f32 v148, v128, v64, s17
	v_cvt_scalef32_pk_fp8_f32 v149, v76, v80, s17
	v_cvt_scalef32_pk_fp8_f32 v150, v92, v96, s17
	v_cvt_scalef32_pk_fp8_f32 v151, v108, v112, s17
	v_cvt_scalef32_pk_fp8_f32 v148, v68, v72, s17 op_sel:[0,0,0,1]
	v_cvt_scalef32_pk_fp8_f32 v149, v84, v88, s17 op_sel:[0,0,0,1]
	v_cvt_scalef32_pk_fp8_f32 v150, v100, v104, s17 op_sel:[0,0,0,1]
	s_waitcnt vmcnt(20)
	v_cvt_scalef32_pk_fp8_f32 v151, v116, v124, s17 op_sel:[0,0,0,1]
	ds_write_b128 v141, v[148:151] offset:32768
	v_mov_b32_e32 v148, v123
	v_mov_b32_e32 v149, v123
	v_mov_b32_e32 v150, v123
	v_mov_b32_e32 v151, v123
	v_cvt_scalef32_pk_fp8_f32 v148, v129, v65, s17
	v_cvt_scalef32_pk_fp8_f32 v149, v77, v81, s17
	v_cvt_scalef32_pk_fp8_f32 v150, v93, v97, s17
	v_cvt_scalef32_pk_fp8_f32 v151, v109, v113, s17
	v_cvt_scalef32_pk_fp8_f32 v148, v69, v73, s17 op_sel:[0,0,0,1]
	v_cvt_scalef32_pk_fp8_f32 v149, v85, v89, s17 op_sel:[0,0,0,1]
	v_cvt_scalef32_pk_fp8_f32 v150, v101, v105, s17 op_sel:[0,0,0,1]
	v_cvt_scalef32_pk_fp8_f32 v151, v117, v125, s17 op_sel:[0,0,0,1]
	ds_write_b128 v141, v[148:151] offset:32896
	v_mov_b32_e32 v148, v123
	v_mov_b32_e32 v149, v123
	v_mov_b32_e32 v150, v123
	v_mov_b32_e32 v151, v123
	v_mov_b32_e32 v120, v123
	v_mov_b32_e32 v121, v123
	v_mov_b32_e32 v122, v123
	v_cvt_scalef32_pk_fp8_f32 v148, v130, v66, s17
	v_cvt_scalef32_pk_fp8_f32 v149, v78, v82, s17
	v_cvt_scalef32_pk_fp8_f32 v150, v94, v98, s17
	v_cvt_scalef32_pk_fp8_f32 v151, v110, v114, s17
	v_cvt_scalef32_pk_fp8_f32 v120, v131, v67, s17
	v_cvt_scalef32_pk_fp8_f32 v121, v79, v83, s17
	v_cvt_scalef32_pk_fp8_f32 v122, v95, v99, s17
	v_cvt_scalef32_pk_fp8_f32 v123, v111, v115, s17
	v_cvt_scalef32_pk_fp8_f32 v148, v70, v74, s17 op_sel:[0,0,0,1]
	v_cvt_scalef32_pk_fp8_f32 v149, v86, v90, s17 op_sel:[0,0,0,1]
	v_cvt_scalef32_pk_fp8_f32 v150, v102, v106, s17 op_sel:[0,0,0,1]
	v_cvt_scalef32_pk_fp8_f32 v151, v118, v126, s17 op_sel:[0,0,0,1]
	v_cvt_scalef32_pk_fp8_f32 v120, v71, v75, s17 op_sel:[0,0,0,1]
	v_cvt_scalef32_pk_fp8_f32 v121, v87, v91, s17 op_sel:[0,0,0,1]
	v_cvt_scalef32_pk_fp8_f32 v122, v103, v107, s17 op_sel:[0,0,0,1]
	v_cvt_scalef32_pk_fp8_f32 v123, v119, v127, s17 op_sel:[0,0,0,1]
	s_add_u32 s30, s0, 0x8000
	ds_write_b128 v142, v[148:151] offset:32768
	ds_write_b128 v143, v[120:123] offset:32768
	s_waitcnt lgkmcnt(0)
	s_barrier
	s_addc_u32 s31, s1, 0
	ds_read_b128 v[64:67], v152 offset:32768
	ds_read_b128 v[68:71], v152 offset:33792
	ds_read_b128 v[72:75], v152 offset:34816
	ds_read_b128 v[76:79], v152 offset:35840
	s_nop 3
	s_waitcnt lgkmcnt(3)
	global_store_dwordx4 v137, v[64:67], s[30:31] sc1
	s_waitcnt lgkmcnt(2)
	global_store_dwordx4 v138, v[68:71], s[30:31] sc1
	s_waitcnt lgkmcnt(1)
	global_store_dwordx4 v139, v[72:75], s[30:31] sc1
	s_waitcnt lgkmcnt(0)
	global_store_dwordx4 v140, v[76:79], s[30:31] sc1
	s_nop 1
	s_add_u32 s0, s0, 0x10000
	s_addc_u32 s1, s1, 0
	s_mov_b64 s[30:31], 0x200000
	s_cmp_lt_u32 s14, 14
	v_lshl_add_u64 v[134:135], v[134:135], 0, s[30:31]
	s_cbranch_scc1 .LBB0_589
